# MoE experts 8-9 fp8 conversion moved from phase 0 into the idle tail of the in-projection phase on the 120 workgroups with one bf16 tile fewer (copy of the per-wave converter)
# speedup vs baseline: 1.0280x; 1.0054x over previous
.LBB0_5:
	s_or_b64 exec, exec, s[0:1]
	s_cmp_lt_i32 s82, 1
	s_cselect_b64 s[0:1], -1, 0
	s_cmp_gt_i32 s83, 0
	s_cselect_b64 s[4:5], -1, 0
	s_and_b64 s[16:17], s[0:1], s[4:5]
	s_andn2_b64 vcc, exec, s[16:17]
	s_cbranch_vccnz .LBB0_231
	s_lshl_b32 s26, s2, 3
	s_add_i32 s2, s2, 0x300
	s_cmpk_gt_i32 s2, 0x6df
	s_mov_b64 s[10:11], s[86:87]
	s_barrier
	s_cbranch_scc1 .LBB0_168
	s_add_u32 s27, s80, 0x1d00000
	s_addc_u32 s28, s81, 0
	s_add_u32 s29, s80, 0x1100000
	s_addc_u32 s30, s81, 0
	s_add_u32 s31, s80, 0x1500000
	s_addc_u32 s33, s81, 0
	s_and_b32 s18, s2, 1
	s_cmp_eq_u32 s18, 0
	s_cselect_b64 s[0:1], -1, 0
	s_add_u32 s35, s80, 0x1000000
	s_addc_u32 s36, s81, 0
	s_add_u32 s37, s80, 0x2500000
	s_addc_u32 s38, s81, 0
	s_add_u32 s39, s80, 0x74700000
	s_addc_u32 s40, s81, 0
	s_add_u32 s41, s80, 0x24e00000
	s_addc_u32 s42, s81, 0
	s_add_u32 s43, s80, 0x4e00000
	s_addc_u32 s44, s81, 0
	v_lshlrev_b32_e32 v1, 2, v253
	v_lshrrev_b32_e32 v2, 2, v253
	v_or_b32_e32 v3, 0x200, v253
	v_or_b32_e32 v4, 0x400, v253
	v_or_b32_e32 v66, 0x600, v253
	v_lshrrev_b32_e32 v130, 4, v253
	v_or_b32_e32 v5, 0xa00, v253
	s_cmpk_gt_i32 s2, 0x2ff
	v_or_b32_e32 v6, 0xe00, v253
	s_cbranch_scc0 .LBB0_13
	s_cmpk_gt_u32 s2, 0x58f
	s_cbranch_scc0 .LBB0_14
	s_lshl_b32 s4, s2, 4
	s_and_b32 s12, s4, 0x7f80
	s_cmpk_gt_u32 s2, 0x59f
	s_cbranch_scc0 .LBB0_15
	s_lshl_b32 s5, s2, 8
	s_and_b32 s13, s5, 0x700
	s_lshl_b32 s14, s13, 11
	s_cmpk_gt_u32 s2, 0x61f
	s_cbranch_scc0 .LBB0_17
	s_cmpk_gt_u32 s2, 0x65f
	s_cbranch_scc0 .LBB0_18
	s_and_b32 s4, s4, 0x7fffff80
	s_addk_i32 s4, 0x9a00
	s_mov_b32 s5, 0
	s_lshl_b64 s[6:7], s[4:5], 13
	s_load_dwordx2 s[8:9], s[10:11], 0xc8
	s_add_u32 s5, s27, s14
	s_addc_u32 s15, s28, 0
	s_add_u32 s4, s5, s4
	s_addc_u32 s5, s15, 0
	s_waitcnt lgkmcnt(0)
	s_add_u32 s6, s8, s6
	s_addc_u32 s7, s9, s7
	s_lshl_b32 s8, s13, 2
	s_add_u32 s8, s6, s8
	s_addc_u32 s9, s7, 0
	s_mov_b64 s[6:7], 0
	s_branch .LBB0_19

.LBB0_168:
	s_sub_i32 s2, s2, 0x300
	v_lshl_or_b32 v2, s2, 9, v253
	s_movk_i32 s0, 0x2900
	v_cmp_gt_i32_e32 vcc, s0, v2
	s_and_saveexec_b64 s[0:1], vcc
	s_cbranch_execz .LBB0_187
	s_lshl_b32 s4, s3, 9
	v_ashrrev_i32_e32 v3, 31, v2
	v_lshl_add_u64 v[4:5], v[2:3], 2, s[80:81]
	s_mov_b64 s[6:7], 0xa00000
	s_ashr_i32 s5, s4, 31
	v_lshl_add_u64 v[4:5], v[4:5], 0, s[6:7]
	s_lshl_b64 s[6:7], s[4:5], 2
	s_mov_b64 s[8:9], 0
	s_movk_i32 s5, 0x7ff
	s_movk_i32 s22, 0xbff
	s_movk_i32 s23, 0x1bff
	s_movk_i32 s24, 0x1c0f
	s_movk_i32 s25, 0x1cff
	v_mov_b32_e32 v7, 0
	s_movk_i32 s27, 0x28ff
	s_branch .LBB0_171

.LBB0_479:
	s_cmpk_lt_u32 s2, 0x88
	s_cbranch_scc1 .Lp2t_skip
	s_mov_b64 s[28:29], s[4:5]
	s_lshr_b32 s33, s92, 6
	v_mbcnt_lo_u32_b32 v65, -1, 0
	v_mbcnt_hi_u32_b32 v65, -1, v65
	s_mov_b64 s[16:17], s[86:87]
	s_mov_b64 s[18:19], s[80:81]
	s_mov_b32 s8, s33
	s_sub_i32 s0, s2, 0x88
	s_lshl_b32 s0, s0, 3
	s_add_i32 s20, s8, s0
	s_cmpk_gt_i32 s20, 0x17ff
	s_cbranch_scc1 .Lp2t_end
	s_add_i32 s0, s20, 0x11000
	s_add_i32 s14, s20, 0x4000
	s_cmpk_lt_i32 s20, 0x1000
	s_cselect_b32 s9, s14, s0
	s_cmp_gt_i32 s9, 0xffff
	s_cbranch_scc0 .Lp2t_1227
	s_load_dwordx2 s[0:1], s[16:17], 0x110
	s_add_i32 s4, s9, 0xffff0000
	s_mov_b32 s7, 0
	s_lshr_b32 s6, s4, 10
	s_lshl_b64 s[4:5], s[6:7], 24
	s_waitcnt lgkmcnt(0)
	s_add_u32 s0, s0, s4
	s_addc_u32 s1, s1, s5
	s_lshl_b32 s4, s9, 1
	s_and_b32 s10, s4, 0x780
	s_lshl_b32 s4, s10, 13
	s_add_u32 s0, s0, s4
	s_addc_u32 s1, s1, 0
	s_lshl_b32 s4, s9, 5
	s_and_b32 s11, s4, 0x7e0
	s_lshl_b32 s4, s11, 2
	s_add_u32 s4, s0, s4
	s_addc_u32 s5, s1, 0
	s_lshl_b64 s[0:1], s[6:7], 22
	s_lshl_b32 s6, s11, 11
	s_add_u32 s0, s18, s0
	s_addc_u32 s1, s19, s1
	s_add_u32 s0, s0, s6
	s_addc_u32 s1, s1, 0
	s_add_u32 s0, s0, s10
	s_addc_u32 s1, s1, 0
	s_add_u32 s0, s0, 0x24e00000
	s_addc_u32 s1, s1, 0
	s_mov_b32 s21, 0x42800000
	s_cbranch_execz .Lp2t_1228
	s_branch .Lp2t_1229

.Lp2t_1229:
	v_lshlrev_b32_e32 v0, 2, v65
	v_lshrrev_b32_e32 v64, 3, v65
	v_and_b32_e32 v128, 28, v0
	v_mov_b32_e32 v131, 0
	v_lshlrev_b32_e32 v130, 2, v128
	v_lshlrev_b32_e32 v132, 17, v64
	v_lshl_add_u64 v[56:57], s[4:5], 0, v[130:131]
	v_mov_b32_e32 v133, v131
	v_or_b32_e32 v134, 0x2000, v132
	v_mov_b32_e32 v135, v131
	v_or_b32_e32 v136, 0x4000, v132
	v_mov_b32_e32 v137, v131
	v_or_b32_e32 v138, 0x6000, v132
	v_mov_b32_e32 v139, v131
	v_or_b32_e32 v140, 0x8000, v132
	v_mov_b32_e32 v141, v131
	v_or_b32_e32 v142, 0xa000, v132
	v_mov_b32_e32 v143, v131
	v_or_b32_e32 v144, 0xc000, v132
	v_mov_b32_e32 v145, v131
	v_or_b32_e32 v146, 0xe000, v132
	v_mov_b32_e32 v147, v131
	v_or_b32_e32 v148, 0x10000, v132
	v_mov_b32_e32 v149, v131
	v_or_b32_e32 v150, 0x12000, v132
	v_mov_b32_e32 v151, v131
	v_or_b32_e32 v152, 0x14000, v132
	v_mov_b32_e32 v153, v131
	v_or_b32_e32 v154, 0x16000, v132
	v_mov_b32_e32 v155, v131
	v_or_b32_e32 v156, 0x18000, v132
	v_mov_b32_e32 v157, v131
	v_or_b32_e32 v158, 0x1a000, v132
	v_mov_b32_e32 v159, v131
	v_or_b32_e32 v160, 0x1c000, v132
	v_mov_b32_e32 v161, v131
	v_lshl_add_u64 v[8:9], v[56:57], 0, v[132:133]
	v_lshl_add_u64 v[10:11], v[56:57], 0, v[134:135]
	v_lshl_add_u64 v[16:17], v[56:57], 0, v[136:137]
	v_lshl_add_u64 v[18:19], v[56:57], 0, v[138:139]
	v_lshl_add_u64 v[24:25], v[56:57], 0, v[140:141]
	v_lshl_add_u64 v[26:27], v[56:57], 0, v[142:143]
	v_lshl_add_u64 v[32:33], v[56:57], 0, v[144:145]
	v_lshl_add_u64 v[34:35], v[56:57], 0, v[146:147]
	v_lshl_add_u64 v[40:41], v[56:57], 0, v[148:149]
	v_lshl_add_u64 v[42:43], v[56:57], 0, v[150:151]
	v_lshl_add_u64 v[48:49], v[56:57], 0, v[152:153]
	v_lshl_add_u64 v[50:51], v[56:57], 0, v[154:155]
	v_lshl_add_u64 v[58:59], v[56:57], 0, v[156:157]
	v_lshl_add_u64 v[60:61], v[56:57], 0, v[158:159]
	v_lshl_add_u64 v[66:67], v[56:57], 0, v[160:161]
	v_or_b32_e32 v162, 0x1e000, v132
	v_mov_b32_e32 v163, v131
	global_load_dwordx4 v[0:3], v[8:9], off nt
	global_load_dwordx4 v[4:7], v[10:11], off nt
	s_nop 0
	global_load_dwordx4 v[8:11], v[16:17], off nt
	global_load_dwordx4 v[12:15], v[18:19], off nt
	s_nop 0
	global_load_dwordx4 v[16:19], v[24:25], off nt
	global_load_dwordx4 v[20:23], v[26:27], off nt
	s_nop 0
	global_load_dwordx4 v[24:27], v[32:33], off nt
	global_load_dwordx4 v[28:31], v[34:35], off nt
	s_nop 0
	global_load_dwordx4 v[32:35], v[40:41], off nt
	global_load_dwordx4 v[36:39], v[42:43], off nt
	s_nop 0
	global_load_dwordx4 v[40:43], v[48:49], off nt
	global_load_dwordx4 v[44:47], v[50:51], off nt
	s_nop 0
	global_load_dwordx4 v[48:51], v[58:59], off nt
	global_load_dwordx4 v[52:55], v[60:61], off nt
	v_lshl_add_u64 v[68:69], v[56:57], 0, v[162:163]
	global_load_dwordx4 v[56:59], v[66:67], off nt
	global_load_dwordx4 v[60:63], v[68:69], off nt
	s_mulk_i32 s8, 0x1200
	s_add_i32 s4, s8, 0
	s_add_i32 s4, s4, 0x14000
	s_movk_i32 s22, 0x3c0
	s_waitcnt lgkmcnt(0)
	s_add_u32 s23, s18, 0x24e00000
	v_lshlrev_b32_e32 v65, 4, v65
	s_addc_u32 s24, s19, 0
	v_and_b32_e32 v164, 0x70, v65
	v_lshl_add_u32 v66, v64, 4, s4
	s_add_u32 s18, s18, 0x4e00000
	v_add_u32_e32 v65, s4, v164
	v_mul_u32_u24_e32 v67, 0x90, v128
	v_mul_u32_u24_e32 v68, 0x90, v64
	v_lshlrev_b32_e32 v166, 11, v64
	s_mov_b32 s5, 0
	s_addc_u32 s19, s19, 0
	v_mov_b32_e32 v165, v131
	v_mov_b32_e32 v167, v131
	v_or_b32_e32 v168, 0x4000, v166
	v_mov_b32_e32 v169, v131
	v_or_b32_e32 v170, 0x8000, v166
	v_mov_b32_e32 v171, v131
	v_or_b32_e32 v172, 0xc000, v166
	v_mov_b32_e32 v173, v131
	s_movk_i32 s25, 0xf0
	v_add_u32_e32 v129, v66, v67
	v_add_u32_e32 v174, v65, v68
	s_mov_b64 s[6:7], s[0:1]
	s_mov_b32 s26, s21
	s_branch .Lp2t_1233

.Lp2t_1233:
	s_add_i32 s20, s20, s22
	s_cmpk_lt_i32 s20, 0x1800
	s_cselect_b64 s[8:9], -1, 0
	s_cmpk_gt_i32 s20, 0x17ff
	s_cbranch_scc1 .Lp2t_1239
	s_add_i32 s0, s20, 0x11000
	s_add_i32 s14, s20, 0x4000
	s_cmpk_lt_i32 s20, 0x1000
	s_cselect_b32 s27, s14, s0
	s_cmp_gt_i32 s27, 0xffff
	s_mov_b64 s[12:13], -1
	s_cbranch_scc0 .Lp2t_1236
	s_load_dwordx2 s[0:1], s[16:17], 0x110
	s_add_i32 s4, s27, 0xffff0000
	s_lshr_b32 s4, s4, 10
	s_lshl_b64 s[10:11], s[4:5], 24
	s_waitcnt lgkmcnt(0)
	s_add_u32 s0, s0, s10
	s_addc_u32 s1, s1, s11
	s_lshl_b32 s10, s27, 1
	s_and_b32 s12, s10, 0x780
	s_lshl_b32 s10, s12, 13
	s_add_u32 s0, s0, s10
	s_addc_u32 s1, s1, 0
	s_lshl_b32 s10, s27, 5
	s_and_b32 s13, s10, 0x7e0
	s_lshl_b32 s10, s13, 2
	s_add_u32 s10, s0, s10
	s_addc_u32 s11, s1, 0
	s_lshl_b64 s[0:1], s[4:5], 22
	s_lshl_b32 s4, s13, 11
	s_add_u32 s0, s23, s0
	s_addc_u32 s1, s24, s1
	s_add_u32 s0, s0, s4
	s_addc_u32 s1, s1, 0
	s_add_u32 s0, s0, s12
	s_addc_u32 s1, s1, 0
	s_mov_b64 s[12:13], 0

.Lp2t_1239:
	s_waitcnt vmcnt(15)
	v_mul_f32_e32 v130, s26, v0
	s_waitcnt vmcnt(14)
	v_mul_f32_e32 v175, s26, v4
	v_mov_b32_e32 v176, v131
	v_cvt_pk_fp8_f32 v176, v130, v175
	s_waitcnt vmcnt(11)
	v_mul_f32_e32 v130, s26, v16
	s_waitcnt vmcnt(10)
	v_mul_f32_e32 v175, s26, v20
	v_mov_b32_e32 v177, v131
	v_cvt_pk_fp8_f32 v177, v130, v175
	v_mul_f32_e32 v178, s26, v8
	v_mul_f32_e32 v179, s26, v12
	s_waitcnt vmcnt(9)
	v_mul_f32_e32 v130, s26, v24
	s_waitcnt vmcnt(8)
	v_mul_f32_e32 v175, s26, v28
	v_cvt_pk_fp8_f32 v176, v178, v179 op_sel:[0,0,1]
	v_cvt_pk_fp8_f32 v177, v130, v175 op_sel:[0,0,1]
	s_waitcnt vmcnt(7)
	v_mul_f32_e32 v130, s26, v32
	s_waitcnt vmcnt(6)
	v_mul_f32_e32 v175, s26, v36
	v_mov_b32_e32 v178, v131
	v_cvt_pk_fp8_f32 v178, v130, v175
	s_waitcnt vmcnt(3)
	v_mul_f32_e32 v130, s26, v48
	s_waitcnt vmcnt(2)
	v_mul_f32_e32 v175, s26, v52
	v_mov_b32_e32 v179, v131
	v_cvt_pk_fp8_f32 v179, v130, v175
	v_mul_f32_e32 v180, s26, v40
	v_mul_f32_e32 v181, s26, v44
	s_waitcnt vmcnt(1)
	v_mul_f32_e32 v130, s26, v56
	s_waitcnt vmcnt(0)
	v_mul_f32_e32 v175, s26, v60
	v_cvt_pk_fp8_f32 v178, v180, v181 op_sel:[0,0,1]
	v_cvt_pk_fp8_f32 v179, v130, v175 op_sel:[0,0,1]
	v_mul_f32_e32 v130, s26, v1
	v_mul_f32_e32 v175, s26, v5
	v_mov_b32_e32 v180, v131
	v_cvt_pk_fp8_f32 v180, v130, v175
	v_mul_f32_e32 v130, s26, v17
	v_mul_f32_e32 v175, s26, v21
	v_mov_b32_e32 v181, v131
	v_cvt_pk_fp8_f32 v181, v130, v175
	v_mul_f32_e32 v182, s26, v9
	v_mul_f32_e32 v183, s26, v13
	v_mul_f32_e32 v130, s26, v25
	v_mul_f32_e32 v175, s26, v29
	v_cvt_pk_fp8_f32 v180, v182, v183 op_sel:[0,0,1]
	v_cvt_pk_fp8_f32 v181, v130, v175 op_sel:[0,0,1]
	v_mul_f32_e32 v130, s26, v33
	v_mul_f32_e32 v175, s26, v37
	v_mov_b32_e32 v182, v131
	v_cvt_pk_fp8_f32 v182, v130, v175
	v_mul_f32_e32 v130, s26, v49
	v_mul_f32_e32 v175, s26, v53
	v_mov_b32_e32 v183, v131
	v_cvt_pk_fp8_f32 v183, v130, v175
	v_mul_f32_e32 v184, s26, v41
	v_mul_f32_e32 v185, s26, v45
	v_mul_f32_e32 v130, s26, v57
	v_mul_f32_e32 v175, s26, v61
	v_cvt_pk_fp8_f32 v182, v184, v185 op_sel:[0,0,1]
	v_cvt_pk_fp8_f32 v183, v130, v175 op_sel:[0,0,1]
	v_mul_f32_e32 v130, s26, v2
	v_mul_f32_e32 v175, s26, v6
	v_mov_b32_e32 v184, v131
	v_cvt_pk_fp8_f32 v184, v130, v175
	v_mul_f32_e32 v130, s26, v18
	v_mul_f32_e32 v175, s26, v22
	v_mov_b32_e32 v185, v131
	v_cvt_pk_fp8_f32 v185, v130, v175
	v_mul_f32_e32 v186, s26, v10
	v_mul_f32_e32 v187, s26, v14
	v_mul_f32_e32 v130, s26, v26
	v_mul_f32_e32 v175, s26, v30
	v_cvt_pk_fp8_f32 v184, v186, v187 op_sel:[0,0,1]
	v_cvt_pk_fp8_f32 v185, v130, v175 op_sel:[0,0,1]
	v_mul_f32_e32 v130, s26, v34
	v_mul_f32_e32 v175, s26, v38
	v_mov_b32_e32 v186, v131
	v_cvt_pk_fp8_f32 v186, v130, v175
	v_mul_f32_e32 v130, s26, v50
	v_mul_f32_e32 v175, s26, v54
	v_mov_b32_e32 v187, v131
	v_cvt_pk_fp8_f32 v187, v130, v175
	v_mul_f32_e32 v188, s26, v42
	v_mul_f32_e32 v189, s26, v46
	v_mul_f32_e32 v130, s26, v58
	v_mul_f32_e32 v175, s26, v62
	v_cvt_pk_fp8_f32 v186, v188, v189 op_sel:[0,0,1]
	v_cvt_pk_fp8_f32 v187, v130, v175 op_sel:[0,0,1]
	v_mul_f32_e32 v130, s26, v3
	v_mul_f32_e32 v175, s26, v7
	v_mov_b32_e32 v188, v131
	v_cvt_pk_fp8_f32 v188, v130, v175
	v_mul_f32_e32 v130, s26, v19
	v_mul_f32_e32 v175, s26, v23
	v_mov_b32_e32 v189, v131
	v_cvt_pk_fp8_f32 v189, v130, v175
	v_mul_f32_e32 v190, s26, v11
	v_mul_f32_e32 v191, s26, v15
	v_mul_f32_e32 v130, s26, v27
	v_mul_f32_e32 v175, s26, v31
	v_cvt_pk_fp8_f32 v188, v190, v191 op_sel:[0,0,1]
	v_cvt_pk_fp8_f32 v189, v130, v175 op_sel:[0,0,1]
	v_mul_f32_e32 v130, s26, v35
	v_mul_f32_e32 v175, s26, v39
	v_mov_b32_e32 v190, v131
	v_cvt_pk_fp8_f32 v190, v130, v175
	v_mul_f32_e32 v130, s26, v51
	v_mul_f32_e32 v175, s26, v55
	v_mov_b32_e32 v191, v131
	v_cvt_pk_fp8_f32 v191, v130, v175
	v_mul_f32_e32 v192, s26, v43
	v_mul_f32_e32 v193, s26, v47
	v_mul_f32_e32 v130, s26, v59
	v_mul_f32_e32 v175, s26, v63
	v_cvt_pk_fp8_f32 v190, v192, v193 op_sel:[0,0,1]
	v_cvt_pk_fp8_f32 v191, v130, v175 op_sel:[0,0,1]
	ds_write_b128 v129, v[176:179]
	ds_write_b128 v129, v[180:183] offset:144
	ds_write_b128 v129, v[184:187] offset:288
	ds_write_b128 v129, v[188:191] offset:432
	s_waitcnt lgkmcnt(0)
	ds_read_b128 v[176:179], v174
	ds_read_b128 v[180:183], v174 offset:1152
	v_lshl_add_u64 v[188:189], s[6:7], 0, v[164:165]
	v_lshl_add_u64 v[184:185], v[188:189], 0, v[166:167]
	v_lshl_add_u64 v[190:191], v[188:189], 0, v[168:169]
	s_waitcnt lgkmcnt(1)
	global_store_dwordx4 v[184:185], v[176:179], off nt
	ds_read_b128 v[176:179], v174 offset:2304
	ds_read_b128 v[184:187], v174 offset:3456
	s_waitcnt lgkmcnt(2)
	global_store_dwordx4 v[190:191], v[180:183], off nt
	s_andn2_b64 vcc, exec, s[8:9]
	s_mov_b64 s[8:9], -1
	v_lshl_add_u64 v[180:181], v[188:189], 0, v[170:171]
	s_waitcnt lgkmcnt(1)
	global_store_dwordx4 v[180:181], v[176:179], off nt
	s_nop 1
	v_lshl_add_u64 v[176:177], v[188:189], 0, v[172:173]
	s_waitcnt lgkmcnt(0)
	global_store_dwordx4 v[176:177], v[184:187], off nt
	s_waitcnt lgkmcnt(0)
	s_cbranch_vccnz .Lp2t_1232
	s_add_i32 s27, s20, s22
	s_cmpk_gt_i32 s27, 0x17ff
	s_cselect_b64 s[8:9], -1, 0
	s_and_b64 vcc, exec, s[8:9]
	s_cbranch_vccnz .Lp2t_1231
	s_add_i32 s4, s27, 0x11000
	s_add_i32 s14, s27, 0x4000
	s_cmpk_lt_i32 s27, 0x1000
	s_cselect_b32 s20, s14, s4
	s_cmp_gt_i32 s20, 0xffff
	s_mov_b64 s[12:13], -1
	s_cbranch_scc0 .Lp2t_1243
	s_load_dwordx2 s[6:7], s[16:17], 0x110
	s_add_i32 s4, s20, 0xffff0000
	s_lshr_b32 s4, s4, 10
	s_lshl_b64 s[10:11], s[4:5], 24
	s_waitcnt lgkmcnt(0)
	s_add_u32 s6, s6, s10
	s_addc_u32 s7, s7, s11
	s_lshl_b32 s10, s20, 1
	s_and_b32 s12, s10, 0x780
	s_lshl_b32 s10, s12, 13
	s_add_u32 s6, s6, s10
	s_addc_u32 s7, s7, 0
	s_lshl_b32 s10, s20, 5
	s_and_b32 s13, s10, 0x7e0
	s_lshl_b32 s10, s13, 2
	s_add_u32 s10, s6, s10
	s_addc_u32 s11, s7, 0
	s_lshl_b64 s[6:7], s[4:5], 22
	s_lshl_b32 s4, s13, 11
	s_add_u32 s6, s23, s6
	s_addc_u32 s7, s24, s7
	s_add_u32 s4, s6, s4
	s_addc_u32 s7, s7, 0
	s_add_u32 s6, s4, s12
	s_addc_u32 s7, s7, 0
	s_mov_b64 s[12:13], 0

.Lp2t_end:
	s_waitcnt vmcnt(0) lgkmcnt(0)
	s_mov_b64 s[4:5], s[28:29]
